# branch-projection skinny GEMM epilogues: gate/addend pieces requested at the top of the unit, eight partial sums read from LDS together
# speedup vs baseline: 1.0109x; 1.0109x over previous
; #define LAS __attribute__((address_space(3)))
; template <class Epi>
; DI void skinny64(const bf16* A, int lda, const bf16* Bt, int ldb, int N, int K, int r0, LAS unsigned char* lds, const Epi& epi, int wave, int lane, int bid, int G) {
;     const int n16 = lane & 15, q = lane >> 4; const int ksw = (K / 32) / 8;
;     LAS f32x4* red = (LAS f32x4*)lds;
;     for (int uu = bid; uu < (N / 16) * 2; uu += G) { const int nt = uu >> 1, mh = uu & 1;
;         f32x4 acc[2];
; #pragma unroll
;         for (int mt = 0; mt < 2; ++mt) acc[mt] = (f32x4){0.f, 0.f, 0.f, 0.f};
;         const bf16* wp = Bt + (size_t)(16 * nt + n16) * ldb + 8 * q + wave * ksw * 32; const bf16* ap = A + (size_t)(r0 + 32 * mh + n16) * lda + 8 * q + wave * ksw * 32;
; #pragma unroll 8
;         for (int ks = 0; ks < ksw; ++ks) { const bf16x8 wf = *(const bf16x8*)(wp + ks * 32);
; #pragma unroll
;             for (int mt = 0; mt < 2; ++mt) acc[mt] = __builtin_amdgcn_mfma_f32_16x16x32_bf16(wf, *(const bf16x8*)(ap + (size_t)(16 * mt) * lda + ks * 32), acc[mt], 0, 0, 0); }
;         __syncthreads();
; #pragma unroll
;         for (int mt = 0; mt < 2; ++mt) red[(wave * 2 + mt) * 64 + lane] = acc[mt];
;         __syncthreads();
;         if (wave < 2) { f32x4 s = red[wave * 64 + lane];
; #pragma unroll
;             for (int w = 1; w < 8; ++w) s = s + red[(w * 2 + wave) * 64 + lane];
;             epi(r0 + 32 * mh + 16 * wave + n16, 16 * nt + 4 * q, s); }
.LBB0_1410:
	s_and_b32 s24, s4, -16
	v_or_b32_e32 v6, s24, v12
	v_ashrrev_i32_e32 v7, 31, v6
	s_and_b32 s25, s2, 32
	v_lshlrev_b64 v[6:7], 11, v[6:7]
	s_bitset1_b32 s25, 13
	s_andn2_b64 vcc, exec, s[12:13]
	s_cbranch_vccnz .Lsk1_np
	v_or_b32_e32 v234, s24, v15
	v_add_u32_e32 v236, s25, v14
	v_mov_b64_e32 v[238:239], s[40:41]
	v_ashrrev_i32_e32 v235, 31, v234
	v_mad_i64_i32 v[238:239], s[82:83], v236, s15, v[238:239]
	v_lshlrev_b64 v[234:235], 1, v[234:235]
	v_lshl_add_u64 v[238:239], v[238:239], 0, v[234:235]
	global_load_dwordx2 v[240:241], v[238:239], off offset:3072
.Lsk1_np:
	v_lshl_add_u64 v[10:11], v[2:3], 0, v[6:7]
	v_or_b32_e32 v6, s25, v12
	v_lshlrev_b32_e32 v90, 11, v6
	v_lshl_add_u64 v[28:29], v[4:5], 0, v[90:91]
	s_mov_b32 s26, 0x8000
	v_add_co_u32_e32 v30, vcc, s26, v28
	global_load_dwordx4 v[6:9], v[10:11], off
	global_load_dwordx4 v[16:19], v[28:29], off
	v_addc_co_u32_e32 v31, vcc, 0, v29, vcc
	global_load_dwordx4 v[20:23], v[30:31], off
	global_load_dwordx4 v[108:111], v[10:11], off offset:64
	global_load_dwordx4 v[112:115], v[28:29], off offset:64
	global_load_dwordx4 v[116:119], v[30:31], off offset:64
	global_load_dwordx4 v[120:123], v[10:11], off offset:128
	global_load_dwordx4 v[124:127], v[28:29], off offset:128
	global_load_dwordx4 v[128:131], v[30:31], off offset:128
	global_load_dwordx4 v[132:135], v[10:11], off offset:192
	global_load_dwordx4 v[136:139], v[28:29], off offset:192
	global_load_dwordx4 v[140:143], v[30:31], off offset:192
	s_andn2_b64 vcc, exec, s[12:13]
	v_add_u32_e32 v10, s0, v13
	s_waitcnt vmcnt(10)
	v_mfma_f32_16x16x32_bf16 v[16:19], v[6:9], v[16:19], 0
	s_waitcnt vmcnt(9)
	v_mfma_f32_16x16x32_bf16 v[6:9], v[6:9], v[20:23], 0
	s_waitcnt vmcnt(7)
	v_mfma_f32_16x16x32_bf16 v[16:19], v[108:111], v[112:115], v[16:19]
	s_waitcnt vmcnt(6)
	v_mfma_f32_16x16x32_bf16 v[6:9], v[108:111], v[116:119], v[6:9]
	s_waitcnt vmcnt(4)
	v_mfma_f32_16x16x32_bf16 v[16:19], v[120:123], v[124:127], v[16:19]
	s_waitcnt vmcnt(3)
	v_mfma_f32_16x16x32_bf16 v[6:9], v[120:123], v[128:131], v[6:9]
	s_waitcnt vmcnt(1)
	v_mfma_f32_16x16x32_bf16 v[16:19], v[132:135], v[136:139], v[16:19]
	s_barrier
	s_waitcnt vmcnt(0)
	v_mfma_f32_16x16x32_bf16 v[6:9], v[132:135], v[140:143], v[6:9]
	s_nop 4
	ds_write_b128 v10, v[16:19]
	s_nop 2
	ds_write_b128 v10, v[6:9] offset:1024
	s_waitcnt lgkmcnt(0)
	s_barrier
	s_cbranch_vccnz .LBB0_1409
	v_add_u32_e32 v20, s1, v13
	ds_read_b128 v[152:155], v20
	ds_read_b128 v[156:159], v20 offset:2048
	ds_read_b128 v[160:163], v20 offset:4096
	ds_read_b128 v[164:167], v20 offset:6144
	ds_read_b128 v[172:175], v20 offset:8192
	ds_read_b128 v[176:179], v20 offset:10240
	ds_read_b128 v[198:201], v20 offset:12288
	ds_read_b128 v[202:205], v20 offset:14336
	s_waitcnt lgkmcnt(6)
	v_pk_add_f32 v[18:19], v[154:155], v[158:159]
	v_pk_add_f32 v[8:9], v[152:153], v[156:157]
	s_waitcnt lgkmcnt(5)
	v_pk_add_f32 v[18:19], v[18:19], v[162:163]
	v_pk_add_f32 v[8:9], v[8:9], v[160:161]
	s_waitcnt lgkmcnt(4)
	v_pk_add_f32 v[18:19], v[18:19], v[166:167]
	v_pk_add_f32 v[8:9], v[8:9], v[164:165]
	s_waitcnt lgkmcnt(3)
	v_pk_add_f32 v[18:19], v[18:19], v[174:175]
	v_pk_add_f32 v[8:9], v[8:9], v[172:173]
	s_waitcnt lgkmcnt(2)
	v_pk_add_f32 v[18:19], v[18:19], v[178:179]
	v_pk_add_f32 v[8:9], v[8:9], v[176:177]
	s_waitcnt lgkmcnt(1)
	v_pk_add_f32 v[18:19], v[18:19], v[200:201]
	v_pk_add_f32 v[8:9], v[8:9], v[198:199]
	s_waitcnt lgkmcnt(0)
	v_pk_add_f32 v[18:19], v[18:19], v[204:205]
	v_pk_add_f32 v[8:9], v[8:9], v[202:203]
	v_or_b32_e32 v6, s24, v15
	v_add_u32_e32 v10, s25, v14
	v_ashrrev_i32_e32 v7, 31, v6
	v_lshlrev_b64 v[6:7], 1, v[6:7]
	v_ashrrev_i32_e32 v11, 31, v10
	v_lshlrev_b64 v[10:11], 12, v[10:11]
	v_lshl_add_u64 v[10:11], s[8:9], 0, v[10:11]
	v_lshl_add_u64 v[6:7], v[10:11], 0, v[6:7]
	s_waitcnt vmcnt(0)
	v_lshlrev_b32_e32 v20, 16, v240
	v_and_b32_e32 v16, 0xffff0000, v240
	v_mul_f32_e32 v20, 0xbfb8aa3b, v20
	v_mul_f32_e32 v16, 0xbfb8aa3b, v16
	v_exp_f32_e32 v20, v20
	v_exp_f32_e32 v21, v16
	s_nop 0
	v_pk_add_f32 v[20:21], v[20:21], 1.0 op_sel_hi:[1,0]
	s_nop 0
	v_rcp_f32_e32 v21, v21
	v_rcp_f32_e32 v20, v20
	s_nop 0
	v_pk_fma_f32 v[8:9], v[8:9], v[20:21], 0 op_sel_hi:[1,1,0]
	s_nop 0
	v_cvt_pk_bf16_f32 v8, v8, v9
	v_lshlrev_b32_e32 v9, 16, v241
	v_mul_f32_e32 v9, 0xbfb8aa3b, v9
	v_exp_f32_e32 v16, v9
	v_and_b32_e32 v9, 0xffff0000, v241
	v_mul_f32_e32 v9, 0xbfb8aa3b, v9
	v_exp_f32_e32 v17, v9
	s_nop 0
	v_pk_add_f32 v[16:17], v[16:17], 1.0 op_sel_hi:[1,0]
	s_nop 0
	v_rcp_f32_e32 v17, v17
	v_rcp_f32_e32 v16, v16
	s_nop 0
	v_pk_fma_f32 v[16:17], v[18:19], v[16:17], 0 op_sel_hi:[1,1,0]
	s_nop 0
	v_cvt_pk_bf16_f32 v9, v16, v17
	global_store_dwordx2 v[6:7], v[8:9], off
	s_branch .LBB0_1409

; #define LAS __attribute__((address_space(3)))
; template <class Epi>
; DI void skinny64(const bf16* A, int lda, const bf16* Bt, int ldb, int N, int K, int r0, LAS unsigned char* lds, const Epi& epi, int wave, int lane, int bid, int G) {
;     const int n16 = lane & 15, q = lane >> 4; const int ksw = (K / 32) / 8;
;     LAS f32x4* red = (LAS f32x4*)lds;
;     for (int uu = bid; uu < (N / 16) * 2; uu += G) { const int nt = uu >> 1, mh = uu & 1;
;         f32x4 acc[2];
; #pragma unroll
;         for (int mt = 0; mt < 2; ++mt) acc[mt] = (f32x4){0.f, 0.f, 0.f, 0.f};
;         const bf16* wp = Bt + (size_t)(16 * nt + n16) * ldb + 8 * q + wave * ksw * 32; const bf16* ap = A + (size_t)(r0 + 32 * mh + n16) * lda + 8 * q + wave * ksw * 32;
; #pragma unroll 8
;         for (int ks = 0; ks < ksw; ++ks) { const bf16x8 wf = *(const bf16x8*)(wp + ks * 32);
; #pragma unroll
;             for (int mt = 0; mt < 2; ++mt) acc[mt] = __builtin_amdgcn_mfma_f32_16x16x32_bf16(wf, *(const bf16x8*)(ap + (size_t)(16 * mt) * lda + ks * 32), acc[mt], 0, 0, 0); }
;         __syncthreads();
; #pragma unroll
;         for (int mt = 0; mt < 2; ++mt) red[(wave * 2 + mt) * 64 + lane] = acc[mt];
;         __syncthreads();
;         if (wave < 2) { f32x4 s = red[wave * 64 + lane];
; #pragma unroll
;             for (int w = 1; w < 8; ++w) s = s + red[(w * 2 + wave) * 64 + lane];
;             epi(r0 + 32 * mh + 16 * wave + n16, 16 * nt + 4 * q, s); }
.LBB0_1437:
	s_and_b32 s24, s4, -16
	v_or_b32_e32 v6, s24, v18
	v_ashrrev_i32_e32 v7, 31, v6
	s_and_b32 s25, s2, 32
	v_lshlrev_b64 v[6:7], 11, v[6:7]
	s_bitset1_b32 s25, 13
	s_andn2_b64 vcc, exec, s[12:13]
	s_cbranch_vccnz .Lsk2_np
	v_or_b32_e32 v234, s24, v21
	v_add_u32_e32 v236, s25, v20
	v_mov_b64_e32 v[238:239], s[40:41]
	v_ashrrev_i32_e32 v235, 31, v234
	v_mad_i64_i32 v[238:239], s[82:83], v236, s15, v[238:239]
	v_lshlrev_b64 v[234:235], 1, v[234:235]
	v_lshl_add_u64 v[238:239], v[238:239], 0, v[234:235]
	s_movk_i32 s82, 0x1000
	v_add_co_u32_e32 v238, vcc, s82, v238
	v_ashrrev_i32_e32 v237, 31, v236
	s_nop 0
	v_addc_co_u32_e32 v239, vcc, 0, v239, vcc
	global_load_dwordx2 v[240:241], v[238:239], off offset:3072
	v_lshlrev_b64 v[236:237], 12, v[236:237]
	v_lshl_add_u64 v[238:239], s[42:43], 0, v[236:237]
	v_lshl_add_u64 v[238:239], v[238:239], 0, v[234:235]
	global_load_dwordx2 v[242:243], v[238:239], off
.Lsk2_np:
	v_lshl_add_u64 v[26:27], v[2:3], 0, v[6:7]
	v_or_b32_e32 v6, s25, v18
	v_lshlrev_b32_e32 v90, 11, v6
	v_lshl_add_u64 v[28:29], v[4:5], 0, v[90:91]
	s_mov_b32 s26, 0x8000
	v_add_co_u32_e32 v30, vcc, s26, v28
	global_load_dwordx4 v[6:9], v[26:27], off
	global_load_dwordx4 v[10:13], v[28:29], off
	v_addc_co_u32_e32 v31, vcc, 0, v29, vcc
	global_load_dwordx4 v[14:17], v[30:31], off
	global_load_dwordx4 v[108:111], v[26:27], off offset:64
	global_load_dwordx4 v[112:115], v[28:29], off offset:64
	global_load_dwordx4 v[116:119], v[30:31], off offset:64
	global_load_dwordx4 v[120:123], v[26:27], off offset:128
	global_load_dwordx4 v[124:127], v[28:29], off offset:128
	global_load_dwordx4 v[128:131], v[30:31], off offset:128
	global_load_dwordx4 v[132:135], v[26:27], off offset:192
	global_load_dwordx4 v[136:139], v[28:29], off offset:192
	global_load_dwordx4 v[140:143], v[30:31], off offset:192
	s_andn2_b64 vcc, exec, s[12:13]
	s_waitcnt vmcnt(10)
	v_mfma_f32_16x16x32_bf16 v[10:13], v[6:9], v[10:13], 0
	s_waitcnt vmcnt(9)
	v_mfma_f32_16x16x32_bf16 v[6:9], v[6:9], v[14:17], 0
	s_waitcnt vmcnt(7)
	v_mfma_f32_16x16x32_bf16 v[10:13], v[108:111], v[112:115], v[10:13]
	s_waitcnt vmcnt(6)
	v_mfma_f32_16x16x32_bf16 v[6:9], v[108:111], v[116:119], v[6:9]
	s_waitcnt vmcnt(4)
	v_mfma_f32_16x16x32_bf16 v[10:13], v[120:123], v[124:127], v[10:13]
	s_waitcnt vmcnt(3)
	v_mfma_f32_16x16x32_bf16 v[6:9], v[120:123], v[128:131], v[6:9]
	s_waitcnt vmcnt(1)
	v_mfma_f32_16x16x32_bf16 v[10:13], v[132:135], v[136:139], v[10:13]
	s_barrier
	s_waitcnt vmcnt(0)
	v_mfma_f32_16x16x32_bf16 v[6:9], v[132:135], v[140:143], v[6:9]
	s_nop 0
	v_add_u32_e32 v14, s0, v19
	s_nop 2
	ds_write_b128 v14, v[10:13]
	s_nop 2
	ds_write_b128 v14, v[6:9] offset:1024
	s_waitcnt lgkmcnt(0)
	s_barrier
	s_cbranch_vccnz .LBB0_1436
	v_add_u32_e32 v22, s1, v19
	ds_read_b128 v[152:155], v22
	ds_read_b128 v[156:159], v22 offset:2048
	ds_read_b128 v[160:163], v22 offset:4096
	ds_read_b128 v[164:167], v22 offset:6144
	ds_read_b128 v[172:175], v22 offset:8192
	ds_read_b128 v[176:179], v22 offset:10240
	ds_read_b128 v[198:201], v22 offset:12288
	ds_read_b128 v[202:205], v22 offset:14336
	s_waitcnt lgkmcnt(6)
	v_pk_add_f32 v[6:7], v[154:155], v[158:159]
	v_pk_add_f32 v[16:17], v[152:153], v[156:157]
	s_waitcnt lgkmcnt(5)
	v_pk_add_f32 v[6:7], v[6:7], v[162:163]
	v_pk_add_f32 v[16:17], v[16:17], v[160:161]
	s_waitcnt lgkmcnt(4)
	v_pk_add_f32 v[6:7], v[6:7], v[166:167]
	v_pk_add_f32 v[16:17], v[16:17], v[164:165]
	s_waitcnt lgkmcnt(3)
	v_pk_add_f32 v[6:7], v[6:7], v[174:175]
	v_pk_add_f32 v[16:17], v[16:17], v[172:173]
	s_waitcnt lgkmcnt(2)
	v_pk_add_f32 v[6:7], v[6:7], v[178:179]
	v_pk_add_f32 v[16:17], v[16:17], v[176:177]
	s_waitcnt lgkmcnt(1)
	v_pk_add_f32 v[6:7], v[6:7], v[200:201]
	v_pk_add_f32 v[16:17], v[16:17], v[198:199]
	s_waitcnt lgkmcnt(0)
	v_pk_add_f32 v[6:7], v[6:7], v[204:205]
	v_pk_add_f32 v[16:17], v[16:17], v[202:203]
	v_or_b32_e32 v8, s24, v21
	v_add_u32_e32 v10, s25, v20
	v_ashrrev_i32_e32 v9, 31, v8
	v_lshlrev_b64 v[8:9], 1, v[8:9]
	v_ashrrev_i32_e32 v11, 31, v10
	v_lshlrev_b64 v[10:11], 12, v[10:11]
	s_waitcnt vmcnt(0)
	v_lshlrev_b32_e32 v22, 16, v240
	v_and_b32_e32 v14, 0xffff0000, v240
	v_mul_f32_e32 v22, 0xbfb8aa3b, v22
	v_mul_f32_e32 v14, 0xbfb8aa3b, v14
	v_exp_f32_e32 v22, v22
	v_exp_f32_e32 v23, v14
	s_waitcnt vmcnt(0)
	v_lshlrev_b32_e32 v24, 16, v242
	v_and_b32_e32 v25, 0xffff0000, v242
	v_pk_add_f32 v[22:23], v[22:23], 1.0 op_sel_hi:[1,0]
	s_nop 0
	v_rcp_f32_e32 v23, v23
	v_lshlrev_b32_e32 v14, 16, v241
	v_and_b32_e32 v15, 0xffff0000, v241
	v_mul_f32_e32 v14, 0xbfb8aa3b, v14
	v_mul_f32_e32 v15, 0xbfb8aa3b, v15
	v_exp_f32_e32 v14, v14
	v_exp_f32_e32 v15, v15
	v_rcp_f32_e32 v22, v22
	s_nop 0
	v_pk_fma_f32 v[16:17], v[16:17], v[22:23], v[24:25]
	v_pk_add_f32 v[14:15], v[14:15], 1.0 op_sel_hi:[1,0]
	v_cvt_pk_bf16_f32 v12, v16, v17
	v_lshlrev_b32_e32 v16, 16, v243
	v_and_b32_e32 v17, 0xffff0000, v243
	v_rcp_f32_e32 v15, v15
	v_rcp_f32_e32 v14, v14
	s_nop 0
	v_pk_fma_f32 v[6:7], v[6:7], v[14:15], v[16:17]
	s_nop 0
	v_cvt_pk_bf16_f32 v13, v6, v7
	v_lshl_add_u64 v[6:7], s[8:9], 0, v[10:11]
	v_lshl_add_u64 v[6:7], v[6:7], 0, v[8:9]
	global_store_dwordx2 v[6:7], v[12:13], off
	s_branch .LBB0_1436
